# indexer passes B and C2: two keys per exec round-trip (masks kept in SGPR pairs, one exec restore per pair)
# speedup vs baseline: 1.0045x; 1.0045x over previous
.LBB0_718:
	v_lshl_add_u64 v[8:9], v[6:7], 1, s[12:13]
	global_load_dwordx4 v[4:7], v[8:9], off offset:16
	s_nop 0
	global_load_dwordx4 v[8:11], v[8:9], off
	s_and_saveexec_b64 s[24:25], vcc
	s_cbranch_execz .LBB0_845
	ds_read_u16 v2, v49 offset:36864
	v_add_u32_e32 v44, 0x11200, v49
	ds_read_b32 v44, v44
	s_waitcnt vmcnt(6)
	s_waitcnt lgkmcnt(1)
	v_lshrrev_b32_e32 v45, 8, v2
	v_and_b32_e32 v2, 0xff, v2
	v_cndmask_b32_e64 v45, v45, 0, s[22:23]
	v_cndmask_b32_e64 v2, v2, 0, s[22:23]
	s_waitcnt lgkmcnt(0)
	v_add_u32_sdwa v51, v45, v44 dst_sel:DWORD dst_unused:UNUSED_PAD src0_sel:DWORD src1_sel:WORD_1
	v_add_u32_sdwa v214, v2, v44 dst_sel:DWORD dst_unused:UNUSED_PAD src0_sel:DWORD src1_sel:WORD_0
	v_lshl_add_u64 v[44:45], v[40:41], 0, s[16:17]
	v_min_i32_e32 v2, v51, v37
	v_add_u32_e32 v2, v2, v214
	v_add_u32_e32 v51, v53, v51
	s_mov_b64 s[34:35], exec
	v_med3_i32 v214, v51, v52, v36
	v_cmp_eq_u32_sdwa s[30:31], v32, v36 src0_sel:WORD_0 src1_sel:DWORD
	v_cmp_gt_i32_sdwa s[0:1], v32, v214 src0_sel:WORD_0 src1_sel:DWORD
	v_lshl_add_u64 v[56:57], v[2:3], 1, v[38:39]
	v_addc_co_u32_e64 v51, s[30:31], 0, v51, s[30:31]
	v_addc_co_u32_e64 v2, s[30:31], 0, v2, s[0:1]
	v_add_u32_e32 v61, 1, v44
	v_med3_i32 v214, v51, v52, v36
	v_cmp_eq_u32_sdwa s[30:31], v32, v36 src0_sel:WORD_1 src1_sel:DWORD
	v_cmp_gt_i32_sdwa vcc, v32, v214 src0_sel:WORD_1 src1_sel:DWORD
	v_lshl_add_u64 v[58:59], v[2:3], 1, v[38:39]
	v_addc_co_u32_e64 v51, s[30:31], 0, v51, s[30:31]
	v_addc_co_u32_e64 v2, s[30:31], 0, v2, vcc
	s_mov_b64 exec, s[0:1]
	global_store_short v[56:57], v44, off
	s_mov_b64 exec, vcc
	global_store_short v[58:59], v61, off
	s_mov_b64 exec, s[34:35]
	v_lshl_add_u64 v[46:47], v[44:45], 0, 2
	v_med3_i32 v214, v51, v52, v36
	v_cmp_eq_u32_sdwa s[30:31], v33, v36 src0_sel:WORD_0 src1_sel:DWORD
	v_cmp_gt_i32_sdwa s[0:1], v33, v214 src0_sel:WORD_0 src1_sel:DWORD
	v_lshl_add_u64 v[56:57], v[2:3], 1, v[38:39]
	v_addc_co_u32_e64 v51, s[30:31], 0, v51, s[30:31]
	v_addc_co_u32_e64 v2, s[30:31], 0, v2, s[0:1]
	v_add_u32_e32 v61, 3, v44
	v_med3_i32 v214, v51, v52, v36
	v_cmp_eq_u32_sdwa s[30:31], v33, v36 src0_sel:WORD_1 src1_sel:DWORD
	v_cmp_gt_i32_sdwa vcc, v33, v214 src0_sel:WORD_1 src1_sel:DWORD
	v_lshl_add_u64 v[58:59], v[2:3], 1, v[38:39]
	v_addc_co_u32_e64 v51, s[30:31], 0, v51, s[30:31]
	v_addc_co_u32_e64 v2, s[30:31], 0, v2, vcc
	s_mov_b64 exec, s[0:1]
	global_store_short v[56:57], v46, off
	s_mov_b64 exec, vcc
	global_store_short v[58:59], v61, off
	s_mov_b64 exec, s[34:35]
	v_lshl_add_u64 v[32:33], v[44:45], 0, 4
	v_med3_i32 v214, v51, v52, v36
	v_cmp_eq_u32_sdwa s[30:31], v34, v36 src0_sel:WORD_0 src1_sel:DWORD
	v_cmp_gt_i32_sdwa s[0:1], v34, v214 src0_sel:WORD_0 src1_sel:DWORD
	v_lshl_add_u64 v[56:57], v[2:3], 1, v[38:39]
	v_addc_co_u32_e64 v51, s[30:31], 0, v51, s[30:31]
	v_addc_co_u32_e64 v2, s[30:31], 0, v2, s[0:1]
	v_add_u32_e32 v61, 5, v44
	v_med3_i32 v214, v51, v52, v36
	v_cmp_eq_u32_sdwa s[30:31], v34, v36 src0_sel:WORD_1 src1_sel:DWORD
	v_cmp_gt_i32_sdwa vcc, v34, v214 src0_sel:WORD_1 src1_sel:DWORD
	v_lshl_add_u64 v[58:59], v[2:3], 1, v[38:39]
	v_addc_co_u32_e64 v51, s[30:31], 0, v51, s[30:31]
	v_addc_co_u32_e64 v2, s[30:31], 0, v2, vcc
	s_mov_b64 exec, s[0:1]
	global_store_short v[56:57], v32, off
	s_mov_b64 exec, vcc
	global_store_short v[58:59], v61, off
	s_mov_b64 exec, s[34:35]
	v_lshl_add_u64 v[32:33], v[44:45], 0, 6
	v_med3_i32 v214, v51, v52, v36
	v_cmp_eq_u32_sdwa s[30:31], v35, v36 src0_sel:WORD_0 src1_sel:DWORD
	v_cmp_gt_i32_sdwa s[0:1], v35, v214 src0_sel:WORD_0 src1_sel:DWORD
	v_lshl_add_u64 v[56:57], v[2:3], 1, v[38:39]
	v_addc_co_u32_e64 v51, s[30:31], 0, v51, s[30:31]
	v_addc_co_u32_e64 v2, s[30:31], 0, v2, s[0:1]
	v_add_u32_e32 v61, 7, v44
	v_med3_i32 v214, v51, v52, v36
	v_cmp_eq_u32_sdwa s[30:31], v35, v36 src0_sel:WORD_1 src1_sel:DWORD
	v_cmp_gt_i32_sdwa vcc, v35, v214 src0_sel:WORD_1 src1_sel:DWORD
	v_lshl_add_u64 v[58:59], v[2:3], 1, v[38:39]
	v_addc_co_u32_e64 v51, s[30:31], 0, v51, s[30:31]
	v_addc_co_u32_e64 v2, s[30:31], 0, v2, vcc
	s_mov_b64 exec, s[0:1]
	global_store_short v[56:57], v32, off
	s_mov_b64 exec, vcc
	global_store_short v[58:59], v61, off
	s_mov_b64 exec, s[34:35]
	v_lshl_add_u64 v[32:33], v[44:45], 0, 8
	v_med3_i32 v214, v51, v52, v36
	v_cmp_eq_u32_sdwa s[30:31], v28, v36 src0_sel:WORD_0 src1_sel:DWORD
	v_cmp_gt_i32_sdwa s[0:1], v28, v214 src0_sel:WORD_0 src1_sel:DWORD
	v_lshl_add_u64 v[56:57], v[2:3], 1, v[38:39]
	v_addc_co_u32_e64 v51, s[30:31], 0, v51, s[30:31]
	v_addc_co_u32_e64 v2, s[30:31], 0, v2, s[0:1]
	v_add_u32_e32 v61, 9, v44
	v_med3_i32 v214, v51, v52, v36
	v_cmp_eq_u32_sdwa s[30:31], v28, v36 src0_sel:WORD_1 src1_sel:DWORD
	v_cmp_gt_i32_sdwa vcc, v28, v214 src0_sel:WORD_1 src1_sel:DWORD
	v_lshl_add_u64 v[58:59], v[2:3], 1, v[38:39]
	v_addc_co_u32_e64 v51, s[30:31], 0, v51, s[30:31]
	v_addc_co_u32_e64 v2, s[30:31], 0, v2, vcc
	s_mov_b64 exec, s[0:1]
	global_store_short v[56:57], v32, off
	s_mov_b64 exec, vcc
	global_store_short v[58:59], v61, off
	s_mov_b64 exec, s[34:35]
	v_lshl_add_u64 v[32:33], v[44:45], 0, 10
	v_med3_i32 v214, v51, v52, v36
	v_cmp_eq_u32_sdwa s[30:31], v29, v36 src0_sel:WORD_0 src1_sel:DWORD
	v_cmp_gt_i32_sdwa s[0:1], v29, v214 src0_sel:WORD_0 src1_sel:DWORD
	v_lshl_add_u64 v[56:57], v[2:3], 1, v[38:39]
	v_addc_co_u32_e64 v51, s[30:31], 0, v51, s[30:31]
	v_addc_co_u32_e64 v2, s[30:31], 0, v2, s[0:1]
	v_add_u32_e32 v61, 11, v44
	v_med3_i32 v214, v51, v52, v36
	v_cmp_eq_u32_sdwa s[30:31], v29, v36 src0_sel:WORD_1 src1_sel:DWORD
	v_cmp_gt_i32_sdwa vcc, v29, v214 src0_sel:WORD_1 src1_sel:DWORD
	v_lshl_add_u64 v[58:59], v[2:3], 1, v[38:39]
	v_addc_co_u32_e64 v51, s[30:31], 0, v51, s[30:31]
	v_addc_co_u32_e64 v2, s[30:31], 0, v2, vcc
	s_mov_b64 exec, s[0:1]
	global_store_short v[56:57], v32, off
	s_mov_b64 exec, vcc
	global_store_short v[58:59], v61, off
	s_mov_b64 exec, s[34:35]
	v_lshl_add_u64 v[28:29], v[44:45], 0, 12
	v_med3_i32 v214, v51, v52, v36
	v_cmp_eq_u32_sdwa s[30:31], v30, v36 src0_sel:WORD_0 src1_sel:DWORD
	v_cmp_gt_i32_sdwa s[0:1], v30, v214 src0_sel:WORD_0 src1_sel:DWORD
	v_lshl_add_u64 v[56:57], v[2:3], 1, v[38:39]
	v_addc_co_u32_e64 v51, s[30:31], 0, v51, s[30:31]
	v_addc_co_u32_e64 v2, s[30:31], 0, v2, s[0:1]
	v_add_u32_e32 v61, 13, v44
	v_med3_i32 v214, v51, v52, v36
	v_cmp_eq_u32_sdwa s[30:31], v30, v36 src0_sel:WORD_1 src1_sel:DWORD
	v_cmp_gt_i32_sdwa vcc, v30, v214 src0_sel:WORD_1 src1_sel:DWORD
	v_lshl_add_u64 v[58:59], v[2:3], 1, v[38:39]
	v_addc_co_u32_e64 v51, s[30:31], 0, v51, s[30:31]
	v_addc_co_u32_e64 v2, s[30:31], 0, v2, vcc
	s_mov_b64 exec, s[0:1]
	global_store_short v[56:57], v28, off
	s_mov_b64 exec, vcc
	global_store_short v[58:59], v61, off
	s_mov_b64 exec, s[34:35]
	v_lshl_add_u64 v[28:29], v[44:45], 0, 14
	v_med3_i32 v214, v51, v52, v36
	v_cmp_gt_i32_sdwa s[0:1], v31, v214 src0_sel:WORD_0 src1_sel:DWORD
	v_cmp_eq_u32_sdwa s[30:31], v31, v36 src0_sel:WORD_0 src1_sel:DWORD
	v_lshl_add_u64 v[32:33], v[2:3], 1, v[38:39]
	s_and_saveexec_b64 s[34:35], s[0:1]
	global_store_short v[32:33], v28, off
	s_mov_b64 exec, s[34:35]
	v_addc_co_u32_e64 v2, vcc, 0, v2, s[0:1]
	v_addc_co_u32_e64 v51, vcc, 0, v51, s[30:31]
	v_med3_i32 v214, v51, v52, v36
	v_cmp_gt_i32_sdwa s[30:31], v31, v214 src0_sel:WORD_1 src1_sel:DWORD
	v_lshl_add_u64 v[28:29], v[2:3], 1, v[38:39]
	v_or_b32_e32 v214, 15, v44
	s_and_saveexec_b64 s[34:35], s[30:31]
	global_store_short v[28:29], v214, off
	s_mov_b64 exec, s[34:35]
.LBB0_843:
.LBB0_844:
.LBB0_845:
	s_or_b64 exec, exec, s[24:25]
	s_andn2_b64 vcc, exec, s[18:19]
	s_cbranch_vccnz .LBB0_975
	ds_read_u16 v2, v50 offset:36896
	s_waitcnt lgkmcnt(0)
	v_cmp_ne_u16_e32 vcc, 0, v2
	s_and_saveexec_b64 s[18:19], vcc
	s_cbranch_execz .LBB0_973
	ds_read_u16 v2, v49 offset:36896
	s_waitcnt vmcnt(7)
	v_add_u32_e32 v28, 0x11220, v49
	ds_read_b32 v28, v28
	v_lshl_add_u64 v[30:31], v[40:41], 0, s[16:17]
	s_waitcnt vmcnt(4)
	s_waitcnt lgkmcnt(1)
	v_lshrrev_b32_e32 v29, 8, v2
	v_and_b32_e32 v2, 0xff, v2
	v_cndmask_b32_e64 v29, v29, 0, s[22:23]
	v_cndmask_b32_e64 v2, v2, 0, s[22:23]
	s_waitcnt lgkmcnt(0)
	v_add_u32_sdwa v34, v29, v28 dst_sel:DWORD dst_unused:UNUSED_PAD src0_sel:DWORD src1_sel:WORD_1
	v_add_u32_sdwa v35, v2, v28 dst_sel:DWORD dst_unused:UNUSED_PAD src0_sel:DWORD src1_sel:WORD_0
	v_lshl_add_u64 v[28:29], v[30:31], 0, s[84:85]
	v_min_i32_e32 v2, v34, v37
	v_add_u32_e32 v2, v2, v35
	v_add_u32_e32 v34, v53, v34
	s_mov_b64 s[30:31], exec
	v_med3_i32 v35, v34, v52, v36
	v_cmp_eq_u32_sdwa s[24:25], v24, v36 src0_sel:WORD_0 src1_sel:DWORD
	v_cmp_gt_i32_sdwa s[0:1], v24, v35 src0_sel:WORD_0 src1_sel:DWORD
	v_lshl_add_u64 v[56:57], v[2:3], 1, v[38:39]
	v_addc_co_u32_e64 v34, s[24:25], 0, v34, s[24:25]
	v_addc_co_u32_e64 v2, s[24:25], 0, v2, s[0:1]
	v_add_u32_e32 v61, 0x101, v30
	v_med3_i32 v35, v34, v52, v36
	v_cmp_eq_u32_sdwa s[24:25], v24, v36 src0_sel:WORD_1 src1_sel:DWORD
	v_cmp_gt_i32_sdwa vcc, v24, v35 src0_sel:WORD_1 src1_sel:DWORD
	v_lshl_add_u64 v[58:59], v[2:3], 1, v[38:39]
	v_addc_co_u32_e64 v34, s[24:25], 0, v34, s[24:25]
	v_addc_co_u32_e64 v2, s[24:25], 0, v2, vcc
	s_mov_b64 exec, s[0:1]
	global_store_short v[56:57], v28, off
	s_mov_b64 exec, vcc
	global_store_short v[58:59], v61, off
	s_mov_b64 exec, s[30:31]
	v_add_u32_e32 v32, 0x102, v30
	v_med3_i32 v35, v34, v52, v36
	v_cmp_eq_u32_sdwa s[24:25], v25, v36 src0_sel:WORD_0 src1_sel:DWORD
	v_cmp_gt_i32_sdwa s[0:1], v25, v35 src0_sel:WORD_0 src1_sel:DWORD
	v_lshl_add_u64 v[56:57], v[2:3], 1, v[38:39]
	v_addc_co_u32_e64 v34, s[24:25], 0, v34, s[24:25]
	v_addc_co_u32_e64 v2, s[24:25], 0, v2, s[0:1]
	v_add_u32_e32 v61, 0x103, v30
	v_med3_i32 v35, v34, v52, v36
	v_cmp_eq_u32_sdwa s[24:25], v25, v36 src0_sel:WORD_1 src1_sel:DWORD
	v_cmp_gt_i32_sdwa vcc, v25, v35 src0_sel:WORD_1 src1_sel:DWORD
	v_lshl_add_u64 v[58:59], v[2:3], 1, v[38:39]
	v_addc_co_u32_e64 v34, s[24:25], 0, v34, s[24:25]
	v_addc_co_u32_e64 v2, s[24:25], 0, v2, vcc
	s_mov_b64 exec, s[0:1]
	global_store_short v[56:57], v32, off
	s_mov_b64 exec, vcc
	global_store_short v[58:59], v61, off
	s_mov_b64 exec, s[30:31]
	v_add_u32_e32 v24, 0x104, v30
	v_med3_i32 v35, v34, v52, v36
	v_cmp_eq_u32_sdwa s[24:25], v26, v36 src0_sel:WORD_0 src1_sel:DWORD
	v_cmp_gt_i32_sdwa s[0:1], v26, v35 src0_sel:WORD_0 src1_sel:DWORD
	v_lshl_add_u64 v[56:57], v[2:3], 1, v[38:39]
	v_addc_co_u32_e64 v34, s[24:25], 0, v34, s[24:25]
	v_addc_co_u32_e64 v2, s[24:25], 0, v2, s[0:1]
	v_add_u32_e32 v61, 0x105, v30
	v_med3_i32 v35, v34, v52, v36
	v_cmp_eq_u32_sdwa s[24:25], v26, v36 src0_sel:WORD_1 src1_sel:DWORD
	v_cmp_gt_i32_sdwa vcc, v26, v35 src0_sel:WORD_1 src1_sel:DWORD
	v_lshl_add_u64 v[58:59], v[2:3], 1, v[38:39]
	v_addc_co_u32_e64 v34, s[24:25], 0, v34, s[24:25]
	v_addc_co_u32_e64 v2, s[24:25], 0, v2, vcc
	s_mov_b64 exec, s[0:1]
	global_store_short v[56:57], v24, off
	s_mov_b64 exec, vcc
	global_store_short v[58:59], v61, off
	s_mov_b64 exec, s[30:31]
	v_add_u32_e32 v24, 0x106, v30
	v_med3_i32 v35, v34, v52, v36
	v_cmp_eq_u32_sdwa s[24:25], v27, v36 src0_sel:WORD_0 src1_sel:DWORD
	v_cmp_gt_i32_sdwa s[0:1], v27, v35 src0_sel:WORD_0 src1_sel:DWORD
	v_lshl_add_u64 v[56:57], v[2:3], 1, v[38:39]
	v_addc_co_u32_e64 v34, s[24:25], 0, v34, s[24:25]
	v_addc_co_u32_e64 v2, s[24:25], 0, v2, s[0:1]
	v_add_u32_e32 v61, 0x107, v30
	v_med3_i32 v35, v34, v52, v36
	v_cmp_eq_u32_sdwa s[24:25], v27, v36 src0_sel:WORD_1 src1_sel:DWORD
	v_cmp_gt_i32_sdwa vcc, v27, v35 src0_sel:WORD_1 src1_sel:DWORD
	v_lshl_add_u64 v[58:59], v[2:3], 1, v[38:39]
	v_addc_co_u32_e64 v34, s[24:25], 0, v34, s[24:25]
	v_addc_co_u32_e64 v2, s[24:25], 0, v2, vcc
	s_mov_b64 exec, s[0:1]
	global_store_short v[56:57], v24, off
	s_mov_b64 exec, vcc
	global_store_short v[58:59], v61, off
	s_mov_b64 exec, s[30:31]
	v_add_u32_e32 v24, 0x108, v30
	v_med3_i32 v35, v34, v52, v36
	v_cmp_eq_u32_sdwa s[24:25], v20, v36 src0_sel:WORD_0 src1_sel:DWORD
	v_cmp_gt_i32_sdwa s[0:1], v20, v35 src0_sel:WORD_0 src1_sel:DWORD
	v_lshl_add_u64 v[56:57], v[2:3], 1, v[38:39]
	v_addc_co_u32_e64 v34, s[24:25], 0, v34, s[24:25]
	v_addc_co_u32_e64 v2, s[24:25], 0, v2, s[0:1]
	v_add_u32_e32 v61, 0x109, v30
	v_med3_i32 v35, v34, v52, v36
	v_cmp_eq_u32_sdwa s[24:25], v20, v36 src0_sel:WORD_1 src1_sel:DWORD
	v_cmp_gt_i32_sdwa vcc, v20, v35 src0_sel:WORD_1 src1_sel:DWORD
	v_lshl_add_u64 v[58:59], v[2:3], 1, v[38:39]
	v_addc_co_u32_e64 v34, s[24:25], 0, v34, s[24:25]
	v_addc_co_u32_e64 v2, s[24:25], 0, v2, vcc
	s_mov_b64 exec, s[0:1]
	global_store_short v[56:57], v24, off
	s_mov_b64 exec, vcc
	global_store_short v[58:59], v61, off
	s_mov_b64 exec, s[30:31]
	v_add_u32_e32 v24, 0x10a, v30
	v_med3_i32 v35, v34, v52, v36
	v_cmp_eq_u32_sdwa s[24:25], v21, v36 src0_sel:WORD_0 src1_sel:DWORD
	v_cmp_gt_i32_sdwa s[0:1], v21, v35 src0_sel:WORD_0 src1_sel:DWORD
	v_lshl_add_u64 v[56:57], v[2:3], 1, v[38:39]
	v_addc_co_u32_e64 v34, s[24:25], 0, v34, s[24:25]
	v_addc_co_u32_e64 v2, s[24:25], 0, v2, s[0:1]
	v_add_u32_e32 v61, 0x10b, v30
	v_med3_i32 v35, v34, v52, v36
	v_cmp_eq_u32_sdwa s[24:25], v21, v36 src0_sel:WORD_1 src1_sel:DWORD
	v_cmp_gt_i32_sdwa vcc, v21, v35 src0_sel:WORD_1 src1_sel:DWORD
	v_lshl_add_u64 v[58:59], v[2:3], 1, v[38:39]
	v_addc_co_u32_e64 v34, s[24:25], 0, v34, s[24:25]
	v_addc_co_u32_e64 v2, s[24:25], 0, v2, vcc
	s_mov_b64 exec, s[0:1]
	global_store_short v[56:57], v24, off
	s_mov_b64 exec, vcc
	global_store_short v[58:59], v61, off
	s_mov_b64 exec, s[30:31]
	v_add_u32_e32 v20, 0x10c, v30
	v_med3_i32 v35, v34, v52, v36
	v_cmp_eq_u32_sdwa s[24:25], v22, v36 src0_sel:WORD_0 src1_sel:DWORD
	v_cmp_gt_i32_sdwa s[0:1], v22, v35 src0_sel:WORD_0 src1_sel:DWORD
	v_lshl_add_u64 v[56:57], v[2:3], 1, v[38:39]
	v_addc_co_u32_e64 v34, s[24:25], 0, v34, s[24:25]
	v_addc_co_u32_e64 v2, s[24:25], 0, v2, s[0:1]
	v_add_u32_e32 v61, 0x10d, v30
	v_med3_i32 v35, v34, v52, v36
	v_cmp_eq_u32_sdwa s[24:25], v22, v36 src0_sel:WORD_1 src1_sel:DWORD
	v_cmp_gt_i32_sdwa vcc, v22, v35 src0_sel:WORD_1 src1_sel:DWORD
	v_lshl_add_u64 v[58:59], v[2:3], 1, v[38:39]
	v_addc_co_u32_e64 v34, s[24:25], 0, v34, s[24:25]
	v_addc_co_u32_e64 v2, s[24:25], 0, v2, vcc
	s_mov_b64 exec, s[0:1]
	global_store_short v[56:57], v20, off
	s_mov_b64 exec, vcc
	global_store_short v[58:59], v61, off
	s_mov_b64 exec, s[30:31]
	v_add_u32_e32 v20, 0x10e, v30
	v_med3_i32 v35, v34, v52, v36
	v_cmp_gt_i32_sdwa s[0:1], v23, v35 src0_sel:WORD_0 src1_sel:DWORD
	v_cmp_eq_u32_sdwa s[24:25], v23, v36 src0_sel:WORD_0 src1_sel:DWORD
	v_lshl_add_u64 v[24:25], v[2:3], 1, v[38:39]
	s_and_saveexec_b64 s[30:31], s[0:1]
	global_store_short v[24:25], v20, off
	s_mov_b64 exec, s[30:31]
	v_addc_co_u32_e64 v2, vcc, 0, v2, s[0:1]
	v_addc_co_u32_e64 v34, vcc, 0, v34, s[24:25]
	v_med3_i32 v35, v34, v52, v36
	v_cmp_gt_i32_sdwa s[24:25], v23, v35 src0_sel:WORD_1 src1_sel:DWORD
	v_lshl_add_u64 v[20:21], v[2:3], 1, v[38:39]
	v_or_b32_e32 v35, 15, v28
	s_and_saveexec_b64 s[30:31], s[24:25]
	global_store_short v[20:21], v35, off
	s_mov_b64 exec, s[30:31]

.LBB0_976:
	ds_read_u16 v2, v50 offset:36928
	s_waitcnt lgkmcnt(0)
	v_cmp_ne_u16_e32 vcc, 0, v2
	s_and_saveexec_b64 s[18:19], vcc
	s_cbranch_execz .LBB0_1103
	ds_read_u16 v2, v49 offset:36928
	s_waitcnt vmcnt(5)
	v_add_u32_e32 v20, 0x11240, v49
	ds_read_b32 v20, v20
	v_lshl_add_u64 v[22:23], v[40:41], 0, s[16:17]
	s_mov_b64 s[0:1], 0x200
	s_waitcnt lgkmcnt(1)
	v_lshrrev_b32_e32 v21, 8, v2
	v_and_b32_e32 v2, 0xff, v2
	v_cndmask_b32_e64 v21, v21, 0, s[22:23]
	v_cndmask_b32_e64 v2, v2, 0, s[22:23]
	s_waitcnt vmcnt(4) lgkmcnt(0)
	v_add_u32_sdwa v26, v21, v20 dst_sel:DWORD dst_unused:UNUSED_PAD src0_sel:DWORD src1_sel:WORD_1
	v_add_u32_sdwa v27, v2, v20 dst_sel:DWORD dst_unused:UNUSED_PAD src0_sel:DWORD src1_sel:WORD_0
	v_lshl_add_u64 v[20:21], v[22:23], 0, s[0:1]
	s_waitcnt vmcnt(2)
	v_min_i32_e32 v2, v26, v37
	v_add_u32_e32 v2, v2, v27
	v_add_u32_e32 v26, v53, v26
	s_mov_b64 s[28:29], exec
	v_med3_i32 v27, v26, v52, v36
	v_cmp_eq_u32_sdwa s[24:25], v16, v36 src0_sel:WORD_0 src1_sel:DWORD
	v_cmp_gt_i32_sdwa s[0:1], v16, v27 src0_sel:WORD_0 src1_sel:DWORD
	v_lshl_add_u64 v[56:57], v[2:3], 1, v[38:39]
	v_addc_co_u32_e64 v26, s[24:25], 0, v26, s[24:25]
	v_addc_co_u32_e64 v2, s[24:25], 0, v2, s[0:1]
	v_add_u32_e32 v61, 0x201, v22
	v_med3_i32 v27, v26, v52, v36
	v_cmp_eq_u32_sdwa s[24:25], v16, v36 src0_sel:WORD_1 src1_sel:DWORD
	v_cmp_gt_i32_sdwa vcc, v16, v27 src0_sel:WORD_1 src1_sel:DWORD
	v_lshl_add_u64 v[58:59], v[2:3], 1, v[38:39]
	v_addc_co_u32_e64 v26, s[24:25], 0, v26, s[24:25]
	v_addc_co_u32_e64 v2, s[24:25], 0, v2, vcc
	s_mov_b64 exec, s[0:1]
	global_store_short v[56:57], v20, off
	s_mov_b64 exec, vcc
	global_store_short v[58:59], v61, off
	s_mov_b64 exec, s[28:29]
	v_add_u32_e32 v24, 0x202, v22
	v_med3_i32 v27, v26, v52, v36
	v_cmp_eq_u32_sdwa s[24:25], v17, v36 src0_sel:WORD_0 src1_sel:DWORD
	v_cmp_gt_i32_sdwa s[0:1], v17, v27 src0_sel:WORD_0 src1_sel:DWORD
	v_lshl_add_u64 v[56:57], v[2:3], 1, v[38:39]
	v_addc_co_u32_e64 v26, s[24:25], 0, v26, s[24:25]
	v_addc_co_u32_e64 v2, s[24:25], 0, v2, s[0:1]
	v_add_u32_e32 v61, 0x203, v22
	v_med3_i32 v27, v26, v52, v36
	v_cmp_eq_u32_sdwa s[24:25], v17, v36 src0_sel:WORD_1 src1_sel:DWORD
	v_cmp_gt_i32_sdwa vcc, v17, v27 src0_sel:WORD_1 src1_sel:DWORD
	v_lshl_add_u64 v[58:59], v[2:3], 1, v[38:39]
	v_addc_co_u32_e64 v26, s[24:25], 0, v26, s[24:25]
	v_addc_co_u32_e64 v2, s[24:25], 0, v2, vcc
	s_mov_b64 exec, s[0:1]
	global_store_short v[56:57], v24, off
	s_mov_b64 exec, vcc
	global_store_short v[58:59], v61, off
	s_mov_b64 exec, s[28:29]
	v_add_u32_e32 v16, 0x204, v22
	v_med3_i32 v27, v26, v52, v36
	v_cmp_eq_u32_sdwa s[24:25], v18, v36 src0_sel:WORD_0 src1_sel:DWORD
	v_cmp_gt_i32_sdwa s[0:1], v18, v27 src0_sel:WORD_0 src1_sel:DWORD
	v_lshl_add_u64 v[56:57], v[2:3], 1, v[38:39]
	v_addc_co_u32_e64 v26, s[24:25], 0, v26, s[24:25]
	v_addc_co_u32_e64 v2, s[24:25], 0, v2, s[0:1]
	v_add_u32_e32 v61, 0x205, v22
	v_med3_i32 v27, v26, v52, v36
	v_cmp_eq_u32_sdwa s[24:25], v18, v36 src0_sel:WORD_1 src1_sel:DWORD
	v_cmp_gt_i32_sdwa vcc, v18, v27 src0_sel:WORD_1 src1_sel:DWORD
	v_lshl_add_u64 v[58:59], v[2:3], 1, v[38:39]
	v_addc_co_u32_e64 v26, s[24:25], 0, v26, s[24:25]
	v_addc_co_u32_e64 v2, s[24:25], 0, v2, vcc
	s_mov_b64 exec, s[0:1]
	global_store_short v[56:57], v16, off
	s_mov_b64 exec, vcc
	global_store_short v[58:59], v61, off
	s_mov_b64 exec, s[28:29]
	v_add_u32_e32 v16, 0x206, v22
	v_med3_i32 v27, v26, v52, v36
	v_cmp_eq_u32_sdwa s[24:25], v19, v36 src0_sel:WORD_0 src1_sel:DWORD
	v_cmp_gt_i32_sdwa s[0:1], v19, v27 src0_sel:WORD_0 src1_sel:DWORD
	v_lshl_add_u64 v[56:57], v[2:3], 1, v[38:39]
	v_addc_co_u32_e64 v26, s[24:25], 0, v26, s[24:25]
	v_addc_co_u32_e64 v2, s[24:25], 0, v2, s[0:1]
	v_add_u32_e32 v61, 0x207, v22
	v_med3_i32 v27, v26, v52, v36
	v_cmp_eq_u32_sdwa s[24:25], v19, v36 src0_sel:WORD_1 src1_sel:DWORD
	v_cmp_gt_i32_sdwa vcc, v19, v27 src0_sel:WORD_1 src1_sel:DWORD
	v_lshl_add_u64 v[58:59], v[2:3], 1, v[38:39]
	v_addc_co_u32_e64 v26, s[24:25], 0, v26, s[24:25]
	v_addc_co_u32_e64 v2, s[24:25], 0, v2, vcc
	s_mov_b64 exec, s[0:1]
	global_store_short v[56:57], v16, off
	s_mov_b64 exec, vcc
	global_store_short v[58:59], v61, off
	s_mov_b64 exec, s[28:29]
	v_add_u32_e32 v16, 0x208, v22
	v_med3_i32 v27, v26, v52, v36
	v_cmp_eq_u32_sdwa s[24:25], v12, v36 src0_sel:WORD_0 src1_sel:DWORD
	v_cmp_gt_i32_sdwa s[0:1], v12, v27 src0_sel:WORD_0 src1_sel:DWORD
	v_lshl_add_u64 v[56:57], v[2:3], 1, v[38:39]
	v_addc_co_u32_e64 v26, s[24:25], 0, v26, s[24:25]
	v_addc_co_u32_e64 v2, s[24:25], 0, v2, s[0:1]
	v_add_u32_e32 v61, 0x209, v22
	v_med3_i32 v27, v26, v52, v36
	v_cmp_eq_u32_sdwa s[24:25], v12, v36 src0_sel:WORD_1 src1_sel:DWORD
	v_cmp_gt_i32_sdwa vcc, v12, v27 src0_sel:WORD_1 src1_sel:DWORD
	v_lshl_add_u64 v[58:59], v[2:3], 1, v[38:39]
	v_addc_co_u32_e64 v26, s[24:25], 0, v26, s[24:25]
	v_addc_co_u32_e64 v2, s[24:25], 0, v2, vcc
	s_mov_b64 exec, s[0:1]
	global_store_short v[56:57], v16, off
	s_mov_b64 exec, vcc
	global_store_short v[58:59], v61, off
	s_mov_b64 exec, s[28:29]
	v_add_u32_e32 v16, 0x20a, v22
	v_med3_i32 v27, v26, v52, v36
	v_cmp_eq_u32_sdwa s[24:25], v13, v36 src0_sel:WORD_0 src1_sel:DWORD
	v_cmp_gt_i32_sdwa s[0:1], v13, v27 src0_sel:WORD_0 src1_sel:DWORD
	v_lshl_add_u64 v[56:57], v[2:3], 1, v[38:39]
	v_addc_co_u32_e64 v26, s[24:25], 0, v26, s[24:25]
	v_addc_co_u32_e64 v2, s[24:25], 0, v2, s[0:1]
	v_add_u32_e32 v61, 0x20b, v22
	v_med3_i32 v27, v26, v52, v36
	v_cmp_eq_u32_sdwa s[24:25], v13, v36 src0_sel:WORD_1 src1_sel:DWORD
	v_cmp_gt_i32_sdwa vcc, v13, v27 src0_sel:WORD_1 src1_sel:DWORD
	v_lshl_add_u64 v[58:59], v[2:3], 1, v[38:39]
	v_addc_co_u32_e64 v26, s[24:25], 0, v26, s[24:25]
	v_addc_co_u32_e64 v2, s[24:25], 0, v2, vcc
	s_mov_b64 exec, s[0:1]
	global_store_short v[56:57], v16, off
	s_mov_b64 exec, vcc
	global_store_short v[58:59], v61, off
	s_mov_b64 exec, s[28:29]
	v_add_u32_e32 v12, 0x20c, v22
	v_med3_i32 v27, v26, v52, v36
	v_cmp_eq_u32_sdwa s[24:25], v14, v36 src0_sel:WORD_0 src1_sel:DWORD
	v_cmp_gt_i32_sdwa s[0:1], v14, v27 src0_sel:WORD_0 src1_sel:DWORD
	v_lshl_add_u64 v[56:57], v[2:3], 1, v[38:39]
	v_addc_co_u32_e64 v26, s[24:25], 0, v26, s[24:25]
	v_addc_co_u32_e64 v2, s[24:25], 0, v2, s[0:1]
	v_add_u32_e32 v61, 0x20d, v22
	v_med3_i32 v27, v26, v52, v36
	v_cmp_eq_u32_sdwa s[24:25], v14, v36 src0_sel:WORD_1 src1_sel:DWORD
	v_cmp_gt_i32_sdwa vcc, v14, v27 src0_sel:WORD_1 src1_sel:DWORD
	v_lshl_add_u64 v[58:59], v[2:3], 1, v[38:39]
	v_addc_co_u32_e64 v26, s[24:25], 0, v26, s[24:25]
	v_addc_co_u32_e64 v2, s[24:25], 0, v2, vcc
	s_mov_b64 exec, s[0:1]
	global_store_short v[56:57], v12, off
	s_mov_b64 exec, vcc
	global_store_short v[58:59], v61, off
	s_mov_b64 exec, s[28:29]
	v_add_u32_e32 v12, 0x20e, v22
	v_med3_i32 v27, v26, v52, v36
	v_cmp_gt_i32_sdwa s[0:1], v15, v27 src0_sel:WORD_0 src1_sel:DWORD
	v_cmp_eq_u32_sdwa s[24:25], v15, v36 src0_sel:WORD_0 src1_sel:DWORD
	v_lshl_add_u64 v[16:17], v[2:3], 1, v[38:39]
	s_and_saveexec_b64 s[28:29], s[0:1]
	global_store_short v[16:17], v12, off
	s_mov_b64 exec, s[28:29]
	v_addc_co_u32_e64 v2, vcc, 0, v2, s[0:1]
	v_addc_co_u32_e64 v26, vcc, 0, v26, s[24:25]
	v_med3_i32 v27, v26, v52, v36
	v_cmp_gt_i32_sdwa s[24:25], v15, v27 src0_sel:WORD_1 src1_sel:DWORD
	v_lshl_add_u64 v[12:13], v[2:3], 1, v[38:39]
	v_or_b32_e32 v27, 15, v20
	s_and_saveexec_b64 s[28:29], s[24:25]
	global_store_short v[12:13], v27, off
	s_mov_b64 exec, s[28:29]

.LBB0_1104:
	ds_read_u16 v2, v50 offset:36960
	s_waitcnt lgkmcnt(0)
	v_cmp_ne_u16_e32 vcc, 0, v2
	s_and_saveexec_b64 s[18:19], vcc
	s_cbranch_execz .LBB0_710
	ds_read_u16 v2, v49 offset:36960
	s_waitcnt vmcnt(3)
	v_add_u32_e32 v12, 0x11260, v49
	ds_read_b32 v12, v12
	v_lshl_add_u64 v[14:15], v[40:41], 0, s[16:17]
	s_mov_b64 s[0:1], 0x300
	s_waitcnt lgkmcnt(1)
	v_lshrrev_b32_e32 v13, 8, v2
	v_and_b32_e32 v2, 0xff, v2
	v_cndmask_b32_e64 v13, v13, 0, s[22:23]
	v_cndmask_b32_e64 v2, v2, 0, s[22:23]
	s_waitcnt vmcnt(2) lgkmcnt(0)
	v_add_u32_sdwa v18, v13, v12 dst_sel:DWORD dst_unused:UNUSED_PAD src0_sel:DWORD src1_sel:WORD_1
	v_add_u32_sdwa v19, v2, v12 dst_sel:DWORD dst_unused:UNUSED_PAD src0_sel:DWORD src1_sel:WORD_0
	v_lshl_add_u64 v[12:13], v[14:15], 0, s[0:1]
	s_waitcnt vmcnt(0)
	v_min_i32_e32 v2, v18, v37
	v_add_u32_e32 v2, v2, v19
	v_add_u32_e32 v18, v53, v18
	s_mov_b64 s[26:27], exec
	v_med3_i32 v19, v18, v52, v36
	v_cmp_eq_u32_sdwa s[24:25], v8, v36 src0_sel:WORD_0 src1_sel:DWORD
	v_cmp_gt_i32_sdwa s[0:1], v8, v19 src0_sel:WORD_0 src1_sel:DWORD
	v_lshl_add_u64 v[56:57], v[2:3], 1, v[38:39]
	v_addc_co_u32_e64 v18, s[24:25], 0, v18, s[24:25]
	v_addc_co_u32_e64 v2, s[24:25], 0, v2, s[0:1]
	v_add_u32_e32 v61, 0x301, v14
	v_med3_i32 v19, v18, v52, v36
	v_cmp_eq_u32_sdwa s[24:25], v8, v36 src0_sel:WORD_1 src1_sel:DWORD
	v_cmp_gt_i32_sdwa vcc, v8, v19 src0_sel:WORD_1 src1_sel:DWORD
	v_lshl_add_u64 v[58:59], v[2:3], 1, v[38:39]
	v_addc_co_u32_e64 v18, s[24:25], 0, v18, s[24:25]
	v_addc_co_u32_e64 v2, s[24:25], 0, v2, vcc
	s_mov_b64 exec, s[0:1]
	global_store_short v[56:57], v12, off
	s_mov_b64 exec, vcc
	global_store_short v[58:59], v61, off
	s_mov_b64 exec, s[26:27]
	v_add_u32_e32 v16, 0x302, v14
	v_med3_i32 v19, v18, v52, v36
	v_cmp_eq_u32_sdwa s[24:25], v9, v36 src0_sel:WORD_0 src1_sel:DWORD
	v_cmp_gt_i32_sdwa s[0:1], v9, v19 src0_sel:WORD_0 src1_sel:DWORD
	v_lshl_add_u64 v[56:57], v[2:3], 1, v[38:39]
	v_addc_co_u32_e64 v18, s[24:25], 0, v18, s[24:25]
	v_addc_co_u32_e64 v2, s[24:25], 0, v2, s[0:1]
	v_add_u32_e32 v61, 0x303, v14
	v_med3_i32 v19, v18, v52, v36
	v_cmp_eq_u32_sdwa s[24:25], v9, v36 src0_sel:WORD_1 src1_sel:DWORD
	v_cmp_gt_i32_sdwa vcc, v9, v19 src0_sel:WORD_1 src1_sel:DWORD
	v_lshl_add_u64 v[58:59], v[2:3], 1, v[38:39]
	v_addc_co_u32_e64 v18, s[24:25], 0, v18, s[24:25]
	v_addc_co_u32_e64 v2, s[24:25], 0, v2, vcc
	s_mov_b64 exec, s[0:1]
	global_store_short v[56:57], v16, off
	s_mov_b64 exec, vcc
	global_store_short v[58:59], v61, off
	s_mov_b64 exec, s[26:27]
	v_add_u32_e32 v8, 0x304, v14
	v_med3_i32 v19, v18, v52, v36
	v_cmp_eq_u32_sdwa s[24:25], v10, v36 src0_sel:WORD_0 src1_sel:DWORD
	v_cmp_gt_i32_sdwa s[0:1], v10, v19 src0_sel:WORD_0 src1_sel:DWORD
	v_lshl_add_u64 v[56:57], v[2:3], 1, v[38:39]
	v_addc_co_u32_e64 v18, s[24:25], 0, v18, s[24:25]
	v_addc_co_u32_e64 v2, s[24:25], 0, v2, s[0:1]
	v_add_u32_e32 v61, 0x305, v14
	v_med3_i32 v19, v18, v52, v36
	v_cmp_eq_u32_sdwa s[24:25], v10, v36 src0_sel:WORD_1 src1_sel:DWORD
	v_cmp_gt_i32_sdwa vcc, v10, v19 src0_sel:WORD_1 src1_sel:DWORD
	v_lshl_add_u64 v[58:59], v[2:3], 1, v[38:39]
	v_addc_co_u32_e64 v18, s[24:25], 0, v18, s[24:25]
	v_addc_co_u32_e64 v2, s[24:25], 0, v2, vcc
	s_mov_b64 exec, s[0:1]
	global_store_short v[56:57], v8, off
	s_mov_b64 exec, vcc
	global_store_short v[58:59], v61, off
	s_mov_b64 exec, s[26:27]
	v_add_u32_e32 v8, 0x306, v14
	v_med3_i32 v19, v18, v52, v36
	v_cmp_eq_u32_sdwa s[24:25], v11, v36 src0_sel:WORD_0 src1_sel:DWORD
	v_cmp_gt_i32_sdwa s[0:1], v11, v19 src0_sel:WORD_0 src1_sel:DWORD
	v_lshl_add_u64 v[56:57], v[2:3], 1, v[38:39]
	v_addc_co_u32_e64 v18, s[24:25], 0, v18, s[24:25]
	v_addc_co_u32_e64 v2, s[24:25], 0, v2, s[0:1]
	v_add_u32_e32 v61, 0x307, v14
	v_med3_i32 v19, v18, v52, v36
	v_cmp_eq_u32_sdwa s[24:25], v11, v36 src0_sel:WORD_1 src1_sel:DWORD
	v_cmp_gt_i32_sdwa vcc, v11, v19 src0_sel:WORD_1 src1_sel:DWORD
	v_lshl_add_u64 v[58:59], v[2:3], 1, v[38:39]
	v_addc_co_u32_e64 v18, s[24:25], 0, v18, s[24:25]
	v_addc_co_u32_e64 v2, s[24:25], 0, v2, vcc
	s_mov_b64 exec, s[0:1]
	global_store_short v[56:57], v8, off
	s_mov_b64 exec, vcc
	global_store_short v[58:59], v61, off
	s_mov_b64 exec, s[26:27]
	v_add_u32_e32 v8, 0x308, v14
	v_med3_i32 v19, v18, v52, v36
	v_cmp_eq_u32_sdwa s[24:25], v4, v36 src0_sel:WORD_0 src1_sel:DWORD
	v_cmp_gt_i32_sdwa s[0:1], v4, v19 src0_sel:WORD_0 src1_sel:DWORD
	v_lshl_add_u64 v[56:57], v[2:3], 1, v[38:39]
	v_addc_co_u32_e64 v18, s[24:25], 0, v18, s[24:25]
	v_addc_co_u32_e64 v2, s[24:25], 0, v2, s[0:1]
	v_add_u32_e32 v61, 0x309, v14
	v_med3_i32 v19, v18, v52, v36
	v_cmp_eq_u32_sdwa s[24:25], v4, v36 src0_sel:WORD_1 src1_sel:DWORD
	v_cmp_gt_i32_sdwa vcc, v4, v19 src0_sel:WORD_1 src1_sel:DWORD
	v_lshl_add_u64 v[58:59], v[2:3], 1, v[38:39]
	v_addc_co_u32_e64 v18, s[24:25], 0, v18, s[24:25]
	v_addc_co_u32_e64 v2, s[24:25], 0, v2, vcc
	s_mov_b64 exec, s[0:1]
	global_store_short v[56:57], v8, off
	s_mov_b64 exec, vcc
	global_store_short v[58:59], v61, off
	s_mov_b64 exec, s[26:27]
	v_add_u32_e32 v8, 0x30a, v14
	v_med3_i32 v19, v18, v52, v36
	v_cmp_eq_u32_sdwa s[24:25], v5, v36 src0_sel:WORD_0 src1_sel:DWORD
	v_cmp_gt_i32_sdwa s[0:1], v5, v19 src0_sel:WORD_0 src1_sel:DWORD
	v_lshl_add_u64 v[56:57], v[2:3], 1, v[38:39]
	v_addc_co_u32_e64 v18, s[24:25], 0, v18, s[24:25]
	v_addc_co_u32_e64 v2, s[24:25], 0, v2, s[0:1]
	v_add_u32_e32 v61, 0x30b, v14
	v_med3_i32 v19, v18, v52, v36
	v_cmp_eq_u32_sdwa s[24:25], v5, v36 src0_sel:WORD_1 src1_sel:DWORD
	v_cmp_gt_i32_sdwa vcc, v5, v19 src0_sel:WORD_1 src1_sel:DWORD
	v_lshl_add_u64 v[58:59], v[2:3], 1, v[38:39]
	v_addc_co_u32_e64 v18, s[24:25], 0, v18, s[24:25]
	v_addc_co_u32_e64 v2, s[24:25], 0, v2, vcc
	s_mov_b64 exec, s[0:1]
	global_store_short v[56:57], v8, off
	s_mov_b64 exec, vcc
	global_store_short v[58:59], v61, off
	s_mov_b64 exec, s[26:27]
	v_add_u32_e32 v4, 0x30c, v14
	v_med3_i32 v19, v18, v52, v36
	v_cmp_eq_u32_sdwa s[24:25], v6, v36 src0_sel:WORD_0 src1_sel:DWORD
	v_cmp_gt_i32_sdwa s[0:1], v6, v19 src0_sel:WORD_0 src1_sel:DWORD
	v_lshl_add_u64 v[56:57], v[2:3], 1, v[38:39]
	v_addc_co_u32_e64 v18, s[24:25], 0, v18, s[24:25]
	v_addc_co_u32_e64 v2, s[24:25], 0, v2, s[0:1]
	v_add_u32_e32 v61, 0x30d, v14
	v_med3_i32 v19, v18, v52, v36
	v_cmp_eq_u32_sdwa s[24:25], v6, v36 src0_sel:WORD_1 src1_sel:DWORD
	v_cmp_gt_i32_sdwa vcc, v6, v19 src0_sel:WORD_1 src1_sel:DWORD
	v_lshl_add_u64 v[58:59], v[2:3], 1, v[38:39]
	v_addc_co_u32_e64 v18, s[24:25], 0, v18, s[24:25]
	v_addc_co_u32_e64 v2, s[24:25], 0, v2, vcc
	s_mov_b64 exec, s[0:1]
	global_store_short v[56:57], v4, off
	s_mov_b64 exec, vcc
	global_store_short v[58:59], v61, off
	s_mov_b64 exec, s[26:27]
	v_add_u32_e32 v4, 0x30e, v14
	v_med3_i32 v19, v18, v52, v36
	v_cmp_gt_i32_sdwa s[0:1], v7, v19 src0_sel:WORD_0 src1_sel:DWORD
	v_cmp_eq_u32_sdwa s[24:25], v7, v36 src0_sel:WORD_0 src1_sel:DWORD
	v_lshl_add_u64 v[8:9], v[2:3], 1, v[38:39]
	s_and_saveexec_b64 s[26:27], s[0:1]
	global_store_short v[8:9], v4, off
	s_mov_b64 exec, s[26:27]
	v_addc_co_u32_e64 v2, vcc, 0, v2, s[0:1]
	v_addc_co_u32_e64 v18, vcc, 0, v18, s[24:25]
	v_med3_i32 v19, v18, v52, v36
	v_cmp_gt_i32_sdwa s[0:1], v7, v19 src0_sel:WORD_1 src1_sel:DWORD
	v_lshl_add_u64 v[8:9], v[2:3], 1, v[38:39]
	v_or_b32_e32 v19, 15, v12
	s_and_saveexec_b64 s[26:27], s[0:1]
	global_store_short v[8:9], v19, off
	s_branch .LBB0_710
